# baseline (speedup 1.0000x reference)
.LBB1_18:
	s_or_b64 exec, exec, s[4:5]
	v_cvt_pk_f16_f32 v41, v40, v41
	v_cvt_pk_f16_f32 v40, v38, v39
	v_cvt_pk_f16_f32 v38, v62, v63
	v_add_u32_e32 v62, 0x8800, v88
	v_cvt_pk_f16_f32 v37, v36, v37
	v_cvt_pk_f16_f32 v36, v34, v35
	v_cvt_pk_f16_f32 v35, v56, v57
	v_cvt_pk_f16_f32 v34, v54, v55
	ds_write2_b64 v62, v[36:37], v[34:35] offset0:8 offset1:12
	v_cvt_pk_f16_f32 v35, v44, v45
	v_cvt_pk_f16_f32 v34, v42, v43
	v_cvt_pk_f16_f32 v37, v48, v49
	v_cvt_pk_f16_f32 v36, v46, v47
	v_cvt_pk_f16_f32 v39, v64, v65
	ds_write2_b64 v62, v[34:35], v[36:37] offset0:16 offset1:20
	v_cvt_pk_f16_f32 v35, v52, v53
	v_cvt_pk_f16_f32 v34, v50, v51
	v_cvt_pk_f16_f32 v37, v60, v61
	v_cvt_pk_f16_f32 v36, v58, v59
	ds_write2_b64 v62, v[40:41], v[38:39] offset1:4
	ds_write2_b64 v62, v[34:35], v[36:37] offset0:24 offset1:28
	ds_read_b128 v[34:37], v89 offset:34816
	v_add_u32_e32 v44, v80, v82
	v_add_u32_e32 v38, 0xffff9e40, v44
	v_ashrrev_i32_e32 v39, 31, v38
	v_lshlrev_b64 v[38:39], 8, v[38:39]
	v_lshl_add_u64 v[42:43], v[70:71], 0, v[38:39]
	ds_read_b128 v[38:41], v90 offset:34816
	s_waitcnt lgkmcnt(1)
	global_store_dwordx4 v[42:43], v[34:37], off sc1
	v_cmp_lt_i32_e64 s[4:5], s12, v91
	v_add_u32_e32 v67, 0x5e4, v67
	v_add_u32_e32 v34, 0xffff9e44, v44
	v_ashrrev_i32_e32 v35, 31, v34
	v_lshlrev_b64 v[34:35], 8, v[34:35]
	v_lshl_add_u64 v[34:35], v[70:71], 0, v[34:35]
	s_waitcnt lgkmcnt(0)
	global_store_dwordx4 v[34:35], v[38:41], off sc1
	ds_read_b128 v[34:37], v90 offset:35904
	v_add_u32_e32 v82, 0x5e40, v82
	v_add_u32_e32 v38, 0xffff9e48, v44
	v_ashrrev_i32_e32 v39, 31, v38
	v_lshlrev_b64 v[38:39], 8, v[38:39]
	v_lshl_add_u64 v[42:43], v[70:71], 0, v[38:39]
	ds_read_b128 v[38:41], v90 offset:36992
	s_waitcnt lgkmcnt(1)
	global_store_dwordx4 v[42:43], v[34:37], off sc1
	s_or_b64 s[10:11], s[4:5], s[10:11]
	s_waitcnt vmcnt(6)
	v_mov_b64_e32 v[42:43], v[26:27]
	v_add_u32_e32 v34, 0xffff9e4c, v44
	v_ashrrev_i32_e32 v35, 31, v34
	v_lshlrev_b64 v[34:35], 8, v[34:35]
	v_lshl_add_u64 v[34:35], v[70:71], 0, v[34:35]
	s_waitcnt lgkmcnt(0)
	global_store_dwordx4 v[34:35], v[38:41], off sc1
	s_waitcnt vmcnt(5)
	v_mov_b64_e32 v[36:37], v[32:33]
	v_mov_b64_e32 v[34:35], v[30:31]
	v_mov_b64_e32 v[44:45], v[28:29]
	s_waitcnt vmcnt(4)
	v_mov_b64_e32 v[40:41], v[24:25]
	v_mov_b64_e32 v[38:39], v[22:23]
	v_mov_b64_e32 v[48:49], v[16:17]
	v_mov_b64_e32 v[46:47], v[14:15]
	s_andn2_b64 exec, exec, s[10:11]
	s_cbranch_execz .LBB1_21

.LBB2_18:
	s_or_b64 exec, exec, s[12:13]
	v_cvt_pk_f16_f32 v41, v40, v41
	v_cvt_pk_f16_f32 v40, v38, v39
	v_cvt_pk_f16_f32 v38, v62, v63
	v_add_u32_e32 v62, 0x8800, v88
	v_cvt_pk_f16_f32 v37, v36, v37
	v_cvt_pk_f16_f32 v36, v34, v35
	v_cvt_pk_f16_f32 v35, v56, v57
	v_cvt_pk_f16_f32 v34, v54, v55
	ds_write2_b64 v62, v[36:37], v[34:35] offset0:8 offset1:12
	v_cvt_pk_f16_f32 v35, v48, v49
	v_cvt_pk_f16_f32 v34, v46, v47
	v_cvt_pk_f16_f32 v37, v52, v53
	v_cvt_pk_f16_f32 v36, v50, v51
	v_cvt_pk_f16_f32 v39, v64, v65
	ds_write2_b64 v62, v[34:35], v[36:37] offset0:16 offset1:20
	v_cvt_pk_f16_f32 v35, v44, v45
	v_cvt_pk_f16_f32 v34, v42, v43
	v_cvt_pk_f16_f32 v37, v60, v61
	v_cvt_pk_f16_f32 v36, v58, v59
	ds_write2_b64 v62, v[40:41], v[38:39] offset1:4
	ds_write2_b64 v62, v[34:35], v[36:37] offset0:24 offset1:28
	ds_read_b128 v[34:37], v89 offset:34816
	v_add_u32_e32 v44, v81, v82
	v_add_u32_e32 v38, 0x3a80, v44
	v_ashrrev_i32_e32 v39, 31, v38
	v_lshlrev_b64 v[38:39], 8, v[38:39]
	v_lshl_add_u64 v[42:43], v[70:71], 0, v[38:39]
	ds_read_b128 v[38:41], v90 offset:34816
	s_waitcnt lgkmcnt(1)
	global_store_dwordx4 v[42:43], v[34:37], off sc1
	s_and_b64 s[4:5], exec, s[4:5]
	s_or_b64 s[10:11], s[4:5], s[10:11]
	v_add_u32_e32 v34, 0x3a84, v44
	v_ashrrev_i32_e32 v35, 31, v34
	v_lshlrev_b64 v[34:35], 8, v[34:35]
	v_lshl_add_u64 v[34:35], v[70:71], 0, v[34:35]
	s_waitcnt lgkmcnt(0)
	global_store_dwordx4 v[34:35], v[38:41], off sc1
	ds_read_b128 v[34:37], v90 offset:35904
	v_add_u32_e32 v82, 0x5e40, v82
	v_add_u32_e32 v38, 0x3a88, v44
	v_ashrrev_i32_e32 v39, 31, v38
	v_lshlrev_b64 v[38:39], 8, v[38:39]
	v_lshl_add_u64 v[42:43], v[70:71], 0, v[38:39]
	ds_read_b128 v[38:41], v90 offset:36992
	s_waitcnt lgkmcnt(1)
	global_store_dwordx4 v[42:43], v[34:37], off sc1
	s_nop 1
	v_add_u32_e32 v34, 0x3a8c, v44
	v_ashrrev_i32_e32 v35, 31, v34
	v_lshlrev_b64 v[34:35], 8, v[34:35]
	v_lshl_add_u64 v[34:35], v[70:71], 0, v[34:35]
	s_waitcnt lgkmcnt(0)
	global_store_dwordx4 v[34:35], v[38:41], off sc1
	s_waitcnt vmcnt(5)
	v_mov_b64_e32 v[36:37], v[32:33]
	v_mov_b64_e32 v[34:35], v[30:31]
	v_mov_b64_e32 v[32:33], v[24:25]
	v_mov_b64_e32 v[30:31], v[22:23]
	s_waitcnt vmcnt(4)
	v_mov_b64_e32 v[40:41], v[28:29]
	v_mov_b64_e32 v[38:39], v[26:27]
	v_mov_b64_e32 v[28:29], v[16:17]
	v_mov_b64_e32 v[26:27], v[14:15]
	s_andn2_b64 exec, exec, s[10:11]
	s_cbranch_execz .LBB2_21
